# router: the four lazily loaded expert-bias words are loaded with the other bias loads up front; divergent branches only copy
# baseline (speedup 1.0000x reference)
; template <int PH, bool PRB = false>
; __device__ __forceinline__ void run_phase(int layer, LAS unsigned char* lds, const int wv_) {
;     ...
;             if (tid < 64) {
;                 const int t = t0 + tid; float ssq = 0.f;
; #pragma unroll
;                 for (int j = 0; j < 4; ++j) { const f32x4 q = *(const f32x4*)(ssqp + (size_t)t * 16 + 4 * j); ssq += (q[0] + q[1]) + (q[2] + q[3]); }
;                 rs = rsqrtf(ssq * (1.0f / D) + 1e-6f);
;                 float lg[4], le[16];
; #pragma unroll
;                 for (int c = 0; c < 4; ++c) lg[c] = lgt[tid * 33 + c] * rs + bg[c];
; #pragma unroll
;                 for (int c = 0; c < 16; ++c) le[c] = lgt[tid * 33 + 4 + c] * rs + be[c];
;                 int grp = 0; float gm = lg[0];
; #pragma unroll
;                 for (int c = 1; c < 4; ++c) if (lg[c] > gm) { gm = lg[c]; grp = c; }
;                 float gs = 0.f;
; #pragma unroll
;                 for (int c = 0; c < 4; ++c) gs += __expf(lg[c] - gm);
;                 const float ggate = 1.0f / gs;
;                 float es[4];
; #pragma unroll
;                 for (int e = 0; e < 4; ++e) es[e] = grp == 0 ? le[e] : (grp == 1 ? le[4 + e] : (grp == 2 ? le[8 + e] : le[12 + e]));
;                 int i0 = 0; float v0 = es[0];
; #pragma unroll
;                 for (int e = 1; e < 4; ++e) if (es[e] > v0) { v0 = es[e]; i0 = e; }
.LBB0_1449:
	s_nop 6
	ds_write2_b32 v86, v0, v1 offset1:33
	ds_write2_b32 v86, v2, v3 offset0:66 offset1:99
	v_mov_b32_e32 v2, 0
	v_mov_b32_e32 v1, 0
	v_mov_b32_e32 v0, 0
	v_mov_b32_e32 v20, 0
	v_mov_b32_e32 v4, 0
	v_mov_b32_e32 v3, 0
	v_mov_b32_e32 v5, 0
	s_waitcnt lgkmcnt(0)
	s_barrier
	s_and_saveexec_b64 s[44:45], s[6:7]
	s_cbranch_execz .LBB0_1493
	v_add_u32_e32 v0, s50, v83
	v_ashrrev_i32_e32 v1, 31, v0
	v_lshlrev_b64 v[0:1], 6, v[0:1]
	v_lshl_add_u64 v[0:1], s[34:35], 0, v[0:1]
	global_load_dwordx4 v[26:29], v[0:1], off
	global_load_dwordx4 v[30:33], v[0:1], off offset:16
	global_load_dwordx4 v[34:37], v[0:1], off offset:32
	global_load_dwordx4 v[38:41], v[0:1], off offset:48
	s_nop 0
	global_load_dwordx4 v[0:3], v65, s[36:37]
	global_load_dwordx3 v[12:14], v65, s[16:17] offset:4
	global_load_dwordx3 v[8:10], v65, s[16:17] offset:20
	global_load_dwordx3 v[4:6], v65, s[16:17] offset:36
	global_load_dwordx3 v[16:18], v65, s[16:17] offset:52
	global_load_dword v200, v65, s[16:17]
	global_load_dword v201, v65, s[16:17] offset:16
	global_load_dword v202, v65, s[16:17] offset:32
	global_load_dword v203, v65, s[16:17] offset:48
	ds_read2_b32 v[22:23], v87 offset0:7 offset1:11
	ds_read2_b32 v[24:25], v87 offset0:15 offset1:19
	s_waitcnt vmcnt(12)
	v_mov_b32_e32 v20, v27
	v_mov_b32_e32 v21, v28
	v_mov_b32_e32 v27, v29
	s_waitcnt vmcnt(11)
	v_mov_b32_e32 v28, v31
	v_mov_b32_e32 v29, v32
	v_mov_b32_e32 v31, v33
	v_pk_add_f32 v[20:21], v[20:21], v[26:27]
	v_pk_add_f32 v[26:27], v[28:29], v[30:31]
	v_add_f32_e32 v7, v20, v21
	v_pk_add_f32 v[20:21], v[26:27], v[26:27] op_sel:[0,1] op_sel_hi:[1,0]
	s_waitcnt vmcnt(10)
	v_add_f32_e32 v32, v34, v35
	v_add_f32_e32 v34, v36, v37
	s_waitcnt vmcnt(9)
	v_mov_b32_e32 v37, v38
	v_mov_b32_e32 v33, v40
	v_mov_b32_e32 v35, v41
	v_add_f32_e32 v36, 0, v7
	v_mov_b32_e32 v21, v39
	v_pk_add_f32 v[28:29], v[32:33], v[34:35]
	v_pk_add_f32 v[20:21], v[36:37], v[20:21]
	s_nop 0
	v_pk_add_f32 v[20:21], v[20:21], v[28:29]
	ds_read2_b32 v[34:35], v87 offset1:1
	ds_read2_b32 v[36:37], v87 offset0:2 offset1:3
	ds_read2_b32 v[26:27], v87 offset0:5 offset1:6
	ds_read2_b32 v[28:29], v87 offset0:9 offset1:10
	ds_read2_b32 v[32:33], v87 offset0:13 offset1:14
	ds_read2_b32 v[30:31], v87 offset0:17 offset1:18
	v_add_f32_e32 v7, v20, v21
	v_fmamk_f32 v7, v7, 0x3a800000, v218
	v_mul_f32_e32 v11, 0x4b800000, v7
	v_cmp_gt_f32_e32 vcc, s61, v7
	s_nop 1
	v_cndmask_b32_e32 v7, v7, v11, vcc
	v_rsq_f32_e32 v7, v7
	s_nop 0
	v_mul_f32_e32 v11, 0x45800000, v7
	v_cndmask_b32_e32 v20, v7, v11, vcc
	s_waitcnt vmcnt(8) lgkmcnt(5)
	v_pk_fma_f32 v[0:1], v[34:35], v[20:21], v[0:1] op_sel_hi:[1,0,1]
	s_waitcnt lgkmcnt(4)
	v_fma_f32 v7, v36, v20, v2
	v_cmp_gt_f32_e32 vcc, v1, v0
	v_fmac_f32_e32 v3, v37, v20
	s_nop 0
	v_cndmask_b32_e32 v2, v0, v1, vcc
	v_cmp_gt_f32_e64 s[10:11], v7, v2
	s_nop 1
	v_cndmask_b32_e64 v15, v2, v7, s[10:11]
	v_cndmask_b32_e64 v2, 0, 1, vcc
	v_cndmask_b32_e64 v2, v2, 2, s[10:11]
	v_cmp_gt_f32_e32 vcc, v3, v15
	s_nop 1
	v_cndmask_b32_e64 v2, v2, 3, vcc
	v_cmp_lt_i32_e64 s[10:11], 1, v2
	s_and_saveexec_b64 s[12:13], s[10:11]
	s_xor_b64 s[12:13], exec, s[12:13]
	s_cbranch_execz .LBB0_1456
	v_cmp_lt_i32_e64 s[10:11], 2, v2
	s_and_saveexec_b64 s[14:15], s[10:11]
	s_xor_b64 s[10:11], exec, s[14:15]
	s_cbranch_execz .LBB0_1453
	ds_read_b32 v19, v87 offset:64
	s_waitcnt vmcnt(0) lgkmcnt(0)
	v_mov_b32_e32 v11, v203
	v_fmac_f32_e32 v11, v20, v19
.LBB0_1453:
	s_andn2_saveexec_b64 s[10:11], s[10:11]
	s_cbranch_execz .LBB0_1455
	ds_read_b32 v19, v87 offset:48
	s_waitcnt vmcnt(0) lgkmcnt(0)
	v_mov_b32_e32 v11, v202
	v_fmac_f32_e32 v11, v20, v19

; template <int PH, bool PRB = false>
; __device__ __forceinline__ void run_phase(int layer, LAS unsigned char* lds, const int wv_) {
;     ...
;                 float es[4];
; #pragma unroll
;                 for (int e = 0; e < 4; ++e) es[e] = grp == 0 ? le[e] : (grp == 1 ? le[4 + e] : (grp == 2 ? le[8 + e] : le[12 + e]));
;                 int i0 = 0; float v0 = es[0];
; #pragma unroll
;                 for (int e = 1; e < 4; ++e) if (es[e] > v0) { v0 = es[e]; i0 = e; }
.LBB0_1456:
	s_andn2_saveexec_b64 s[12:13], s[12:13]
	s_cbranch_execz .LBB0_1462
	v_cmp_ne_u32_e64 s[10:11], 1, v2
	s_and_saveexec_b64 s[14:15], s[10:11]
	s_xor_b64 s[10:11], exec, s[14:15]
	s_cbranch_execz .LBB0_1459
	ds_read_b32 v19, v87 offset:16
	s_waitcnt vmcnt(0) lgkmcnt(0)
	v_mov_b32_e32 v11, v200
	v_fmac_f32_e32 v11, v20, v19
.LBB0_1459:
	s_andn2_saveexec_b64 s[10:11], s[10:11]
	s_cbranch_execz .LBB0_1461
	ds_read_b32 v19, v87 offset:32
	s_waitcnt vmcnt(0) lgkmcnt(0)
	v_mov_b32_e32 v11, v201
	v_fmac_f32_e32 v11, v20, v19
